# speedup vs baseline: 1.0004x; 1.0004x over previous
_Z10enc_kernelPKfS0_PK15HIP_vector_typeIjLj4EES4_S4_S0_S0_S0_Pf:
	s_load_dwordx4 s[12:15], s[0:1], 0x0
	s_load_dwordx2 s[16:17], s[0:1], 0x10
	s_load_dwordx8 s[4:11], s[0:1], 0x28
	v_lshrrev_b32_e32 v56, 6, v0
	s_lshl_b32 s2, s2, 6
	v_lshl_or_b32 v47, v56, 4, s2
	v_and_b32_e32 v57, 15, v0
	v_or_b32_e32 v2, v47, v57
	v_ashrrev_i32_e32 v3, 31, v2
	s_waitcnt lgkmcnt(0)
	v_and_b32_e32 v119, 48, v0
	global_load_dwordx4 v[120:123], v119, s[4:5]
	global_load_dwordx4 v[124:127], v119, s[4:5] offset:64
	global_load_dwordx4 v[128:131], v119, s[4:5] offset:128
	global_load_dwordx4 v[132:135], v119, s[4:5] offset:192
	global_load_dwordx4 v[136:139], v119, s[4:5] offset:256
	global_load_dwordx4 v[140:143], v119, s[4:5] offset:320
	global_load_dwordx4 v[144:147], v119, s[4:5] offset:384
	global_load_dwordx4 v[148:151], v119, s[4:5] offset:448
	global_load_dwordx4 v[152:155], v119, s[6:7]
	global_load_dwordx4 v[156:159], v119, s[6:7] offset:64
	global_load_dwordx4 v[160:163], v119, s[6:7] offset:128
	global_load_dwordx4 v[164:167], v119, s[6:7] offset:192
	global_load_dwordx4 v[168:171], v119, s[6:7] offset:256
	global_load_dwordx4 v[172:175], v119, s[6:7] offset:320
	global_load_dwordx4 v[176:179], v119, s[8:9]
	global_load_dwordx4 v[180:183], v119, s[8:9] offset:64
	global_load_dwordx4 v[184:187], v119, s[8:9] offset:128
	global_load_dwordx4 v[188:191], v119, s[8:9] offset:192
	v_lshl_add_u64 v[4:5], v[2:3], 2, s[14:15]
	global_load_dword v46, v[4:5], off
	v_mov_b32_e32 v45, 0
	v_lshlrev_b64 v[2:3], 9, v[2:3]
	v_lshlrev_b32_e32 v44, 4, v0
	v_lshl_add_u64 v[2:3], s[12:13], 0, v[2:3]
	v_and_b32_e32 v48, 48, v0
	v_mov_b32_e32 v49, v45
	v_lshl_add_u64 v[4:5], s[16:17], 0, v[44:45]
	v_lshl_add_u64 v[42:43], v[2:3], 0, v[48:49]
	global_load_dwordx4 v[98:101], v[42:43], off
	global_load_dwordx4 v[102:105], v[42:43], off offset:64
	global_load_dwordx4 v[106:109], v[42:43], off offset:128
	global_load_dwordx4 v[110:113], v[42:43], off offset:192
	global_load_dwordx4 v[10:13], v[42:43], off offset:256
	global_load_dwordx4 v[14:17], v[42:43], off offset:320
	s_nop 0
	global_load_dwordx4 v[2:5], v[42:43], off offset:384
	global_load_dwordx4 v[6:9], v[42:43], off offset:448
	v_readfirstlane_b32 s3, v56
	s_lshl_b32 s3, s3, 10
	s_mov_b32 m0, s3
	s_nop 0
	global_load_lds_dwordx4 v44, s[16:17]
	s_add_i32 m0, s3, 0x1000
	s_add_u32 s20, s16, 0x1000
	s_addc_u32 s21, s17, 0
	global_load_lds_dwordx4 v44, s[20:21]
	s_add_i32 m0, s3, 0x2000
	s_add_u32 s20, s16, 0x2000
	s_addc_u32 s21, s17, 0
	global_load_lds_dwordx4 v44, s[20:21]
	s_add_i32 m0, s3, 0x3000
	s_add_u32 s20, s16, 0x3000
	s_addc_u32 s21, s17, 0
	global_load_lds_dwordx4 v44, s[20:21]
	s_add_i32 m0, s3, 0x4000
	s_add_u32 s20, s16, 0x4000
	s_addc_u32 s21, s17, 0
	global_load_lds_dwordx4 v44, s[20:21]
	s_add_i32 m0, s3, 0x5000
	s_add_u32 s20, s16, 0x5000
	s_addc_u32 s21, s17, 0
	global_load_lds_dwordx4 v44, s[20:21]
	s_add_i32 m0, s3, 0x6000
	s_add_u32 s20, s16, 0x6000
	s_addc_u32 s21, s17, 0
	global_load_lds_dwordx4 v44, s[20:21]
	s_add_i32 m0, s3, 0x7000
	s_add_u32 s20, s16, 0x7000
	s_addc_u32 s21, s17, 0
	global_load_lds_dwordx4 v44, s[20:21]
	s_add_i32 m0, s3, 0x8000
	s_add_u32 s20, s16, 0x8000
	s_addc_u32 s21, s17, 0
	global_load_lds_dwordx4 v44, s[20:21]
	s_add_i32 m0, s3, 0x9000
	s_add_u32 s20, s16, 0x9000
	s_addc_u32 s21, s17, 0
	global_load_lds_dwordx4 v44, s[20:21]
	s_add_i32 m0, s3, 0xa000
	s_add_u32 s20, s16, 0xa000
	s_addc_u32 s21, s17, 0
	global_load_lds_dwordx4 v44, s[20:21]
	s_add_i32 m0, s3, 0xb000
	s_add_u32 s20, s16, 0xb000
	s_addc_u32 s21, s17, 0
	global_load_lds_dwordx4 v44, s[20:21]
	s_add_i32 m0, s3, 0xc000
	s_add_u32 s20, s16, 0xc000
	s_addc_u32 s21, s17, 0
	global_load_lds_dwordx4 v44, s[20:21]
	s_add_i32 m0, s3, 0xd000
	s_add_u32 s20, s16, 0xd000
	s_addc_u32 s21, s17, 0
	global_load_lds_dwordx4 v44, s[20:21]
	s_add_i32 m0, s3, 0xe000
	s_add_u32 s20, s16, 0xe000
	s_addc_u32 s21, s17, 0
	global_load_lds_dwordx4 v44, s[20:21]
	s_add_i32 m0, s3, 0xf000
	s_add_u32 s20, s16, 0xf000
	s_addc_u32 s21, s17, 0
	global_load_lds_dwordx4 v44, s[20:21]
	s_add_i32 m0, s3, 0x10000
	s_add_u32 s20, s16, 0x10000
	s_addc_u32 s21, s17, 0
	global_load_lds_dwordx4 v44, s[20:21]
	v_or_b32_e32 v1, 0x10000, v44
	v_and_b32_e32 v49, 63, v0
	s_movk_i32 s0, 0x1040
	s_movk_i32 s2, 0x104
	v_cmp_gt_u32_e32 vcc, 16, v49
	s_waitcnt vmcnt(9)
	s_barrier
	v_mov_b32_e32 v24, v120
	v_mov_b32_e32 v25, v121
	v_mov_b32_e32 v26, v122
	v_mov_b32_e32 v27, v123
	v_mov_b32_e32 v28, v124
	v_mov_b32_e32 v29, v125
	v_mov_b32_e32 v30, v126
	v_mov_b32_e32 v31, v127
	v_mov_b32_e32 v32, v128
	v_mov_b32_e32 v33, v129
	v_mov_b32_e32 v34, v130
	v_mov_b32_e32 v35, v131
	v_mov_b32_e32 v40, v132
	v_mov_b32_e32 v41, v133
	v_mov_b32_e32 v42, v134
	v_mov_b32_e32 v43, v135
	v_pk_fma_f32 v[18:19], v[98:99], -2.0, v[46:47] op_sel_hi:[1,0,0]
	v_pk_fma_f32 v[20:21], v[100:101], -2.0, v[46:47] op_sel_hi:[1,0,0]
	v_pk_fma_f32 v[22:23], v[102:103], -2.0, v[46:47] op_sel_hi:[1,0,0]
	v_pk_fma_f32 v[36:37], v[104:105], -2.0, v[46:47] op_sel_hi:[1,0,0]
	v_pk_fma_f32 v[38:39], v[106:107], -2.0, v[46:47] op_sel_hi:[1,0,0]
	v_cvt_pk_bf16_f32 v18, v18, v19
	v_cvt_pk_bf16_f32 v19, v20, v21
	v_cvt_pk_bf16_f32 v20, v22, v23
	v_cvt_pk_bf16_f32 v21, v36, v37
	v_cvt_pk_bf16_f32 v22, v38, v39
	v_mov_b32_e32 v36, v136
	v_mov_b32_e32 v37, v137
	v_mov_b32_e32 v38, v138
	v_mov_b32_e32 v39, v139
	v_accvgpr_write_b32 a0, v152
	v_accvgpr_write_b32 a1, v153
	v_accvgpr_write_b32 a2, v154
	v_accvgpr_write_b32 a3, v155
	v_accvgpr_write_b32 a4, v160
	v_accvgpr_write_b32 a5, v161
	v_accvgpr_write_b32 a6, v162
	v_accvgpr_write_b32 a7, v163
	v_accvgpr_write_b32 a8, v176
	v_accvgpr_write_b32 a9, v177
	v_accvgpr_write_b32 a10, v178
	v_accvgpr_write_b32 a11, v179
	v_accvgpr_write_b32 a12, v184
	v_accvgpr_write_b32 a13, v185
	v_accvgpr_write_b32 a14, v186
	v_accvgpr_write_b32 a15, v187
	v_lshlrev_b32_e32 v44, 4, v49
	ds_read_b128 v[58:61], v44
	ds_read_b128 v[62:65], v44 offset:1024
	ds_read_b128 v[66:69], v44 offset:4096
	ds_read_b128 v[70:73], v44 offset:5120
	ds_read_b128 v[74:77], v44 offset:8192
	ds_read_b128 v[78:81], v44 offset:9216
	ds_read_b128 v[82:85], v44 offset:12288
	ds_read_b128 v[86:89], v44 offset:13312
	v_pk_fma_f32 v[50:51], v[108:109], -2.0, v[46:47] op_sel_hi:[1,0,0]
	v_pk_fma_f32 v[52:53], v[110:111], -2.0, v[46:47] op_sel_hi:[1,0,0]
	v_pk_fma_f32 v[54:55], v[112:113], -2.0, v[46:47] op_sel_hi:[1,0,0]
	v_cvt_pk_bf16_f32 v23, v50, v51
	v_pk_fma_f32 v[0:1], v[10:11], -2.0, v[46:47] op_sel_hi:[1,0,0]
	v_pk_fma_f32 v[12:13], v[12:13], -2.0, v[46:47] op_sel_hi:[1,0,0]
	v_cvt_pk_bf16_f32 v10, v0, v1
	v_cvt_pk_bf16_f32 v11, v12, v13
	v_pk_fma_f32 v[8:9], v[8:9], -2.0, v[46:47] op_sel_hi:[1,0,0]
	v_pk_mul_f32 v[24:25], v[46:47], v[24:25] op_sel_hi:[0,1]
	v_pk_mul_f32 v[26:27], v[46:47], v[26:27] op_sel_hi:[0,1]
	v_accvgpr_write_b32 a16, v24
	v_accvgpr_write_b32 a17, v25
	v_accvgpr_write_b32 a18, v26
	v_accvgpr_write_b32 a19, v27
	v_pk_mul_f32 v[24:25], v[46:47], v[28:29] op_sel_hi:[0,1]
	v_pk_mul_f32 v[26:27], v[46:47], v[30:31] op_sel_hi:[0,1]
	v_accvgpr_write_b32 a20, v24
	v_accvgpr_write_b32 a21, v25
	v_accvgpr_write_b32 a22, v26
	v_accvgpr_write_b32 a23, v27
	v_pk_mul_f32 v[24:25], v[46:47], v[32:33] op_sel_hi:[0,1]
	v_mov_b32_e32 v30, v140
	v_mov_b32_e32 v31, v141
	v_mov_b32_e32 v32, v142
	v_mov_b32_e32 v33, v143
	v_pk_mul_f32 v[26:27], v[46:47], v[34:35] op_sel_hi:[0,1]
	v_accvgpr_write_b32 a24, v24
	v_accvgpr_write_b32 a25, v25
	v_accvgpr_write_b32 a26, v26
	v_accvgpr_write_b32 a27, v27
	v_pk_mul_f32 v[26:27], v[46:47], v[42:43] op_sel_hi:[0,1]
	v_pk_mul_f32 v[24:25], v[46:47], v[40:41] op_sel_hi:[0,1]
	v_accvgpr_write_b32 a31, v27
	v_accvgpr_write_b32 a30, v26
	v_accvgpr_write_b32 a29, v25
	v_accvgpr_write_b32 a28, v24
	v_pk_fma_f32 v[26:27], v[14:15], -2.0, v[46:47] op_sel_hi:[1,0,0]
	v_pk_fma_f32 v[28:29], v[16:17], -2.0, v[46:47] op_sel_hi:[1,0,0]
	ds_read_b128 v[14:17], v44 offset:2048
	s_waitcnt lgkmcnt(8)
	v_mfma_f32_16x16x32_bf16 a[16:19], v[58:61], v[18:21], a[16:19]
	v_cvt_pk_bf16_f32 v24, v52, v53
	v_cvt_pk_bf16_f32 v25, v54, v55
	v_cvt_pk_bf16_f32 v12, v26, v27
	s_waitcnt lgkmcnt(2)
	v_mfma_f32_16x16x32_bf16 a[28:31], v[82:85], v[18:21], a[28:31]
	v_cvt_pk_bf16_f32 v13, v28, v29
	ds_read_b128 v[26:29], v44 offset:6144
	ds_read_b128 v[40:43], v44 offset:3072
	ds_read_b128 v[50:53], v44 offset:10240
	v_mfma_f32_16x16x32_bf16 a[16:19], v[62:65], v[22:25], a[16:19]
	v_fma_f32 v34, v2, -2.0, v46
	v_fma_f32 v35, v3, -2.0, v46
	v_pk_fma_f32 v[54:55], v[6:7], -2.0, v[46:47] op_sel_hi:[1,0,0]
	v_pk_mul_f32 v[32:33], v[46:47], v[32:33] op_sel_hi:[0,1]
	s_waitcnt lgkmcnt(3)
	v_mfma_f32_16x16x32_bf16 a[16:19], v[14:17], v[10:13], a[16:19]
	ds_read_b128 v[0:3], v44 offset:7168
	ds_read_b128 v[14:17], v44 offset:14336
	v_pk_mul_f32 v[30:31], v[46:47], v[30:31] op_sel_hi:[0,1]
	v_accvgpr_write_b32 a47, v33
	v_mfma_f32_16x16x32_bf16 a[28:31], v[86:89], v[22:25], a[28:31]
	v_accvgpr_write_b32 a46, v32
	v_accvgpr_write_b32 a45, v31
	v_accvgpr_write_b32 a44, v30
	s_waitcnt lgkmcnt(0)
	v_mfma_f32_16x16x32_bf16 a[28:31], v[14:17], v[10:13], a[28:31]
	s_nop 1
	v_mov_b32_e32 v14, v144
	v_mov_b32_e32 v15, v145
	v_mov_b32_e32 v16, v146
	v_mov_b32_e32 v17, v147
	ds_read_b128 v[30:33], v44 offset:23552
	v_accvgpr_write_b32 a56, v156
	v_accvgpr_write_b32 a57, v157
	v_accvgpr_write_b32 a58, v158
	v_accvgpr_write_b32 a59, v159
	v_mfma_f32_16x16x32_bf16 a[20:23], v[66:69], v[18:21], a[20:23]
	v_accvgpr_write_b32 a32, v168
	v_accvgpr_write_b32 a33, v169
	v_accvgpr_write_b32 a34, v170
	v_accvgpr_write_b32 a35, v171
	v_accvgpr_write_b32 a40, v172
	v_accvgpr_write_b32 a41, v173
	v_accvgpr_write_b32 a42, v174
	v_accvgpr_write_b32 a43, v175
	v_mfma_f32_16x16x32_bf16 a[20:23], v[70:73], v[22:25], a[20:23]
	v_mfma_f32_16x16x32_bf16 a[20:23], v[26:29], v[10:13], a[20:23]
	v_fma_f32 v28, v4, -2.0, v46
	v_fma_f32 v29, v5, -2.0, v46
	v_cvt_pk_bf16_f32 v26, v34, v35
	v_cvt_pk_bf16_f32 v27, v28, v29
	v_cvt_pk_bf16_f32 v28, v54, v55
	v_cvt_pk_bf16_f32 v29, v8, v9
	v_mfma_f32_16x16x32_bf16 a[24:27], v[74:77], v[18:21], a[24:27]
	ds_read_b128 v[4:7], v44 offset:11264
	v_pk_mul_f32 v[34:35], v[46:47], v[36:37] op_sel_hi:[0,1]
	v_pk_mul_f32 v[36:37], v[46:47], v[38:39] op_sel_hi:[0,1]
	v_mfma_f32_16x16x32_bf16 a[20:23], v[0:3], v[26:29], a[20:23]
	s_nop 1
	v_mov_b32_e32 v0, v148
	v_mov_b32_e32 v1, v149
	v_mov_b32_e32 v2, v150
	v_mov_b32_e32 v3, v151
	v_accvgpr_write_b32 a39, v37
	v_accvgpr_write_b32 a38, v36
	v_mfma_f32_16x16x32_bf16 a[24:27], v[78:81], v[22:25], a[24:27]
	v_accvgpr_write_b32 a37, v35
	v_accvgpr_write_b32 a36, v34
	ds_read_b128 v[34:37], v44 offset:19456
	v_mfma_f32_16x16x32_bf16 a[24:27], v[50:53], v[10:13], a[24:27]
	ds_read_b128 v[50:53], v44 offset:15360
	v_pk_mul_f32 v[16:17], v[46:47], v[16:17] op_sel_hi:[0,1]
	s_waitcnt lgkmcnt(2)
	v_mfma_f32_16x16x32_bf16 a[24:27], v[4:7], v[26:29], a[24:27]
	ds_read_b128 v[4:7], v44 offset:16384
	v_pk_mul_f32 v[14:15], v[46:47], v[14:15] op_sel_hi:[0,1]
	v_accvgpr_write_b32 a51, v17
	v_mfma_f32_16x16x32_bf16 a[16:19], v[40:43], v[26:29], a[16:19]
	ds_read_b128 v[40:43], v44 offset:17408
	v_accvgpr_write_b32 a50, v16
	v_accvgpr_write_b32 a49, v15
	s_waitcnt lgkmcnt(1)
	v_mfma_f32_16x16x32_bf16 a[36:39], v[4:7], v[18:21], a[36:39]
	ds_read_b128 v[4:7], v44 offset:18432
	v_accvgpr_write_b32 a48, v14
	ds_read_b128 v[14:17], v44 offset:27648
	s_waitcnt lgkmcnt(2)
	v_mfma_f32_16x16x32_bf16 a[36:39], v[40:43], v[22:25], a[36:39]
	v_pk_mul_f32 v[2:3], v[46:47], v[2:3] op_sel_hi:[0,1]
	s_waitcnt lgkmcnt(1)
	v_mfma_f32_16x16x32_bf16 a[36:39], v[4:7], v[10:13], a[36:39]
	ds_read_b128 v[4:7], v44 offset:20480
	v_pk_mul_f32 v[0:1], v[46:47], v[0:1] op_sel_hi:[0,1]
	v_accvgpr_write_b32 a55, v3
	v_mfma_f32_16x16x32_bf16 a[36:39], v[34:37], v[26:29], a[36:39]
	ds_read_b128 v[34:37], v44 offset:21504
	v_accvgpr_write_b32 a54, v2
	v_accvgpr_write_b32 a53, v1
	s_waitcnt lgkmcnt(1)
	v_mfma_f32_16x16x32_bf16 a[44:47], v[4:7], v[18:21], a[44:47]
	ds_read_b128 v[4:7], v44 offset:22528
	v_accvgpr_write_b32 a52, v0
	ds_read_b128 v[0:3], v44 offset:30720
	s_waitcnt lgkmcnt(2)
	v_mfma_f32_16x16x32_bf16 a[44:47], v[34:37], v[22:25], a[44:47]
	v_accvgpr_read_b32 v9, a36
	s_waitcnt lgkmcnt(1)
	v_mfma_f32_16x16x32_bf16 a[44:47], v[4:7], v[10:13], a[44:47]
	ds_read_b128 v[4:7], v44 offset:24576
	v_mfma_f32_16x16x32_bf16 a[44:47], v[30:33], v[26:29], a[44:47]
	ds_read_b128 v[30:33], v44 offset:25600
	s_waitcnt lgkmcnt(1)
	v_mfma_f32_16x16x32_bf16 a[48:51], v[4:7], v[18:21], a[48:51]
	ds_read_b128 v[4:7], v44 offset:26624
	s_waitcnt lgkmcnt(1)
	v_mfma_f32_16x16x32_bf16 a[48:51], v[30:33], v[22:25], a[48:51]
	s_waitcnt lgkmcnt(0)
	v_mfma_f32_16x16x32_bf16 a[48:51], v[4:7], v[10:13], a[48:51]
	ds_read_b128 v[4:7], v44 offset:28672
	v_mfma_f32_16x16x32_bf16 a[48:51], v[14:17], v[26:29], a[48:51]
	ds_read_b128 v[14:17], v44 offset:29696
	s_waitcnt lgkmcnt(1)
	v_mfma_f32_16x16x32_bf16 a[52:55], v[4:7], v[18:21], a[52:55]
	ds_read_b128 v[4:7], v44 offset:31744
	s_nop 3
	v_accvgpr_read_b32 v20, a49
	s_waitcnt lgkmcnt(1)
	v_mfma_f32_16x16x32_bf16 a[52:55], v[14:17], v[22:25], a[52:55]
	v_accvgpr_read_b32 v16, a46
	v_accvgpr_read_b32 v21, a48
	v_cvt_pk_bf16_f32 v20, v21, v20
	v_mfma_f32_16x16x32_bf16 a[52:55], v[0:3], v[10:13], a[52:55]
	v_accvgpr_read_b32 v0, a17
	v_accvgpr_read_b32 v1, a16
	v_cvt_pk_bf16_f32 v0, v1, v0
	v_accvgpr_read_b32 v1, a19
	v_accvgpr_read_b32 v2, a18
	v_mfma_f32_16x16x32_bf16 a[28:31], v[50:53], v[26:29], a[28:31]
	v_cvt_pk_bf16_f32 v1, v2, v1
	v_accvgpr_read_b32 v2, a21
	v_accvgpr_read_b32 v3, a20
	s_waitcnt lgkmcnt(0)
	v_mfma_f32_16x16x32_bf16 a[52:55], v[4:7], v[26:29], a[52:55]
	v_cvt_pk_bf16_f32 v2, v3, v2
	v_accvgpr_read_b32 v3, a23
	v_accvgpr_read_b32 v4, a22
	v_cvt_pk_bf16_f32 v3, v4, v3
	v_accvgpr_read_b32 v4, a25
	v_accvgpr_read_b32 v5, a24
	v_cvt_pk_bf16_f32 v4, v5, v4
	v_accvgpr_read_b32 v5, a27
	v_accvgpr_read_b32 v6, a26
	v_cvt_pk_bf16_f32 v5, v6, v5
	v_accvgpr_read_b32 v6, a29
	v_accvgpr_read_b32 v7, a28
	v_cvt_pk_bf16_f32 v6, v7, v6
	v_accvgpr_read_b32 v7, a31
	v_accvgpr_read_b32 v8, a30
	v_cvt_pk_bf16_f32 v7, v8, v7
	v_accvgpr_read_b32 v8, a37
	s_waitcnt vmcnt(3)
	s_barrier
	ds_read_b128 v[12:15], v44 offset:32768
	v_cvt_pk_bf16_f32 v8, v9, v8
	v_accvgpr_read_b32 v9, a39
	v_accvgpr_read_b32 v10, a38
	v_cvt_pk_bf16_f32 v9, v10, v9
	v_accvgpr_read_b32 v10, a45
	v_accvgpr_read_b32 v11, a44
	v_cvt_pk_bf16_f32 v10, v11, v10
	v_accvgpr_read_b32 v11, a47
	v_cvt_pk_bf16_f32 v11, v16, v11
	ds_read_b128 v[16:19], v44 offset:33792
	ds_read_b128 v[24:27], v44 offset:34816
	s_waitcnt lgkmcnt(2)
	v_mfma_f32_16x16x32_bf16 a[0:3], v[12:15], v[0:3], a[0:3]
	v_accvgpr_read_b32 v21, a51
	v_accvgpr_read_b32 v12, a50
	v_cvt_pk_bf16_f32 v21, v12, v21
	ds_read_b128 v[12:15], v44 offset:35840
	s_waitcnt lgkmcnt(2)
	v_mfma_f32_16x16x32_bf16 a[0:3], v[16:19], v[4:7], a[0:3]
	v_accvgpr_read_b32 v16, a53
	v_accvgpr_read_b32 v17, a52
	v_cvt_pk_bf16_f32 v22, v17, v16
	s_waitcnt lgkmcnt(1)
	v_mfma_f32_16x16x32_bf16 a[0:3], v[24:27], v[8:11], a[0:3]
	v_accvgpr_read_b32 v16, a55
	v_accvgpr_read_b32 v17, a54
	v_accvgpr_write_b32 a16, v164
	v_accvgpr_write_b32 a17, v165
	v_accvgpr_write_b32 a18, v166
	v_accvgpr_write_b32 a19, v167
	v_cvt_pk_bf16_f32 v23, v17, v16
	v_accvgpr_write_b32 a20, v180
	v_accvgpr_write_b32 a21, v181
	v_accvgpr_write_b32 a22, v182
	v_accvgpr_write_b32 a23, v183
	s_waitcnt lgkmcnt(0)
	v_mfma_f32_16x16x32_bf16 a[0:3], v[12:15], v[20:23], a[0:3]
	s_nop 7
	v_accvgpr_read_b32 v12, a0
	v_mul_f32_e32 v12, 0x4038aa3b, v12
	v_exp_f32_e32 v16, v12
	v_accvgpr_read_b32 v12, a1
	v_mul_f32_e32 v12, 0x4038aa3b, v12
	v_exp_f32_e32 v17, v12
	ds_read_b128 v[12:15], v44 offset:36864
	v_add_f32_e32 v16, 1.0, v16
	v_rcp_f32_e32 v28, v16
	v_add_f32_e32 v24, 1.0, v17
	ds_read_b128 v[16:19], v44 offset:37888
	v_rcp_f32_e32 v29, v24
	ds_read_b128 v[24:27], v44 offset:38912
	s_waitcnt lgkmcnt(2)
	v_mfma_f32_16x16x32_bf16 a[24:27], v[12:15], v[0:3], a[56:59]
	v_accvgpr_read_b32 v30, a2
	v_mul_f32_e32 v12, 0x4038aa3b, v30
	v_exp_f32_e32 v30, v12
	ds_read_b128 v[12:15], v44 offset:39936
	s_waitcnt lgkmcnt(2)
	v_mfma_f32_16x16x32_bf16 a[24:27], v[16:19], v[4:7], a[24:27]
	v_accvgpr_read_b32 v16, a3
	v_mul_f32_e32 v16, 0x4038aa3b, v16
	v_exp_f32_e32 v17, v16
	s_waitcnt lgkmcnt(1)
	v_mfma_f32_16x16x32_bf16 a[0:3], v[24:27], v[8:11], a[24:27]
	v_add_f32_e32 v16, 1.0, v30
	v_rcp_f32_e32 v16, v16
	v_add_f32_e32 v17, 1.0, v17
	s_waitcnt lgkmcnt(0)
	v_mfma_f32_16x16x32_bf16 a[0:3], v[12:15], v[20:23], a[0:3]
	v_rcp_f32_e32 v17, v17
	v_pk_fma_f32 v[28:29], v[28:29], -2.0, 1.0 op_sel_hi:[1,0,0]
	v_pk_fma_f32 v[30:31], v[16:17], -2.0, 1.0 op_sel_hi:[1,0,0]
	s_nop 4
	v_accvgpr_read_b32 v12, a0
	v_mul_f32_e32 v12, 0x4038aa3b, v12
	v_accvgpr_read_b32 v13, a1
	v_exp_f32_e32 v12, v12
	v_mul_f32_e32 v13, 0x4038aa3b, v13
	v_exp_f32_e32 v13, v13
	v_accvgpr_read_b32 v35, a3
	v_add_f32_e32 v12, 1.0, v12
	v_rcp_f32_e32 v24, v12
	v_add_f32_e32 v18, 1.0, v13
	ds_read_b128 v[12:15], v44 offset:40960
	v_rcp_f32_e32 v25, v18
	ds_read_b128 v[16:19], v44 offset:41984
	s_waitcnt lgkmcnt(1)
	v_mfma_f32_16x16x32_bf16 a[4:7], v[12:15], v[0:3], a[4:7]
	v_fma_f32 v32, v24, -2.0, 1.0
	v_fma_f32 v33, v25, -2.0, 1.0
	v_accvgpr_read_b32 v24, a2
	v_mul_f32_e32 v34, 0x4038aa3b, v24
	ds_read_b128 v[24:27], v44 offset:43008
	ds_read_b128 v[12:15], v44 offset:44032
	s_waitcnt lgkmcnt(2)
	v_mfma_f32_16x16x32_bf16 a[0:3], v[16:19], v[4:7], a[4:7]
	v_mul_f32_e32 v16, 0x4038aa3b, v35
	v_exp_f32_e32 v16, v16
	v_exp_f32_e32 v34, v34
	s_waitcnt lgkmcnt(1)
	v_mfma_f32_16x16x32_bf16 a[0:3], v[24:27], v[8:11], a[0:3]
	v_add_f32_e32 v16, 1.0, v16
	v_rcp_f32_e32 v35, v16
	v_add_f32_e32 v17, 1.0, v34
	s_waitcnt lgkmcnt(0)
	v_mfma_f32_16x16x32_bf16 a[0:3], v[12:15], v[20:23], a[0:3]
	v_rcp_f32_e32 v34, v17
	v_accvgpr_write_b32 a4, v188
	v_accvgpr_write_b32 a5, v189
	v_accvgpr_write_b32 a6, v190
	v_accvgpr_write_b32 a7, v191
	v_pk_fma_f32 v[34:35], v[34:35], -2.0, 1.0 op_sel_hi:[1,0,0]
	s_nop 4
	v_accvgpr_read_b32 v12, a0
	v_mul_f32_e32 v12, 0x4038aa3b, v12
	v_exp_f32_e32 v16, v12
	v_accvgpr_read_b32 v12, a1
	v_mul_f32_e32 v12, 0x4038aa3b, v12
	v_exp_f32_e32 v17, v12
	ds_read_b128 v[12:15], v44 offset:45056
	v_add_f32_e32 v16, 1.0, v16
	v_rcp_f32_e32 v36, v16
	v_add_f32_e32 v24, 1.0, v17
	ds_read_b128 v[16:19], v44 offset:46080
	v_rcp_f32_e32 v37, v24
	ds_read_b128 v[24:27], v44 offset:47104
	s_waitcnt lgkmcnt(2)
	v_mfma_f32_16x16x32_bf16 a[16:19], v[12:15], v[0:3], a[16:19]
	v_accvgpr_read_b32 v38, a2
	v_mul_f32_e32 v12, 0x4038aa3b, v38
	v_exp_f32_e32 v38, v12
	ds_read_b128 v[12:15], v44 offset:48128
	s_waitcnt lgkmcnt(2)
	v_mfma_f32_16x16x32_bf16 a[16:19], v[16:19], v[4:7], a[16:19]
	v_accvgpr_read_b32 v17, a3
	v_mul_f32_e32 v17, 0x4038aa3b, v17
	v_exp_f32_e32 v17, v17
	s_waitcnt lgkmcnt(1)
	v_mfma_f32_16x16x32_bf16 a[16:19], v[24:27], v[8:11], a[16:19]
	v_add_f32_e32 v16, 1.0, v38
	v_rcp_f32_e32 v38, v16
	v_pk_fma_f32 v[36:37], v[36:37], -2.0, 1.0 op_sel_hi:[1,0,0]
	s_waitcnt lgkmcnt(0)
	v_mfma_f32_16x16x32_bf16 a[0:3], v[12:15], v[20:23], a[16:19]
	v_add_f32_e32 v13, 1.0, v17
	v_rcp_f32_e32 v39, v13
	s_nop 0
	v_pk_fma_f32 v[38:39], v[38:39], -2.0, 1.0 op_sel_hi:[1,0,0]
	s_nop 3
	v_accvgpr_read_b32 v12, a0
	v_mul_f32_e32 v12, 0x4038aa3b, v12
	v_exp_f32_e32 v12, v12
	v_accvgpr_read_b32 v17, a2
	v_mul_f32_e32 v17, 0x4038aa3b, v17
	v_exp_f32_e32 v24, v17
	v_add_f32_e32 v12, 1.0, v12
	v_rcp_f32_e32 v40, v12
	v_accvgpr_read_b32 v12, a1
	v_mul_f32_e32 v12, 0x4038aa3b, v12
	v_exp_f32_e32 v16, v12
	ds_read_b128 v[12:15], v44 offset:49152
	v_add_f32_e32 v42, 1.0, v24
	v_accvgpr_read_b32 v43, a3
	v_add_f32_e32 v25, 1.0, v16
	ds_read_b128 v[16:19], v44 offset:50176
	v_rcp_f32_e32 v41, v25
	ds_read_b128 v[24:27], v44 offset:51200
	s_waitcnt lgkmcnt(2)
	v_mfma_f32_16x16x32_bf16 a[0:3], v[12:15], v[0:3], a[32:35]
	v_mul_f32_e32 v12, 0x4038aa3b, v43
	v_exp_f32_e32 v43, v12
	ds_read_b128 v[12:15], v44 offset:52224
	s_waitcnt lgkmcnt(2)
	v_mfma_f32_16x16x32_bf16 a[0:3], v[16:19], v[4:7], a[0:3]
	v_rcp_f32_e32 v16, v42
	v_add_f32_e32 v17, 1.0, v43
	v_rcp_f32_e32 v17, v17
	s_waitcnt lgkmcnt(1)
	v_mfma_f32_16x16x32_bf16 a[0:3], v[24:27], v[8:11], a[0:3]
	v_fma_f32 v40, v40, -2.0, 1.0
	v_fma_f32 v41, v41, -2.0, 1.0
	v_pk_fma_f32 v[42:43], v[16:17], -2.0, 1.0 op_sel_hi:[1,0,0]
	s_waitcnt lgkmcnt(0)
	v_mfma_f32_16x16x32_bf16 a[0:3], v[12:15], v[20:23], a[0:3]
	s_nop 7
	v_accvgpr_read_b32 v12, a0
	v_mul_f32_e32 v12, 0x4038aa3b, v12
	v_exp_f32_e32 v16, v12
	v_accvgpr_read_b32 v12, a1
	v_mul_f32_e32 v17, 0x4038aa3b, v12
	ds_read_b128 v[12:15], v44 offset:53248
	v_exp_f32_e32 v24, v17
	v_add_f32_e32 v16, 1.0, v16
	v_rcp_f32_e32 v50, v16
	ds_read_b128 v[16:19], v44 offset:54272
	v_add_f32_e32 v24, 1.0, v24
	v_rcp_f32_e32 v51, v24
	ds_read_b128 v[24:27], v44 offset:55296
	s_waitcnt lgkmcnt(2)
	v_mfma_f32_16x16x32_bf16 a[16:19], v[12:15], v[0:3], a[40:43]
	v_accvgpr_read_b32 v52, a2
	v_mul_f32_e32 v0, 0x4038aa3b, v52
	v_exp_f32_e32 v12, v0
	ds_read_b128 v[0:3], v44 offset:56320
	s_waitcnt lgkmcnt(2)
	v_mfma_f32_16x16x32_bf16 a[16:19], v[16:19], v[4:7], a[16:19]
	v_accvgpr_read_b32 v4, a3
	v_mul_f32_e32 v4, 0x4038aa3b, v4
	v_exp_f32_e32 v5, v4
	s_waitcnt lgkmcnt(1)
	v_mfma_f32_16x16x32_bf16 a[0:3], v[24:27], v[8:11], a[16:19]
	v_add_f32_e32 v4, 1.0, v12
	s_waitcnt vmcnt(0)
	s_barrier
	ds_read_b128 v[10:13], v44 offset:57344
	v_add_f32_e32 v5, 1.0, v5
	s_waitcnt lgkmcnt(1)
	v_mfma_f32_16x16x32_bf16 a[0:3], v[0:3], v[20:23], a[0:3]
	v_rcp_f32_e32 v4, v4
	v_rcp_f32_e32 v5, v5
	ds_read_b128 v[18:21], v44 offset:58368
	v_pk_fma_f32 v[14:15], v[50:51], -2.0, 1.0 op_sel_hi:[1,0,0]
	v_cvt_pk_bf16_f32 v6, v36, v37
	v_pk_fma_f32 v[16:17], v[4:5], -2.0, 1.0 op_sel_hi:[1,0,0]
	v_cvt_pk_bf16_f32 v4, v32, v33
	v_cvt_pk_bf16_f32 v5, v34, v35
	v_accvgpr_read_b32 v2, a2
	v_accvgpr_read_b32 v3, a3
	v_mul_f32_e32 v2, 0x4038aa3b, v2
	v_mul_f32_e32 v3, 0x4038aa3b, v3
	v_exp_f32_e32 v2, v2
	v_exp_f32_e32 v3, v3
	v_accvgpr_read_b32 v0, a0
	v_accvgpr_read_b32 v1, a1
	v_add_f32_e32 v2, 1.0, v2
	v_add_f32_e32 v3, 1.0, v3
	v_rcp_f32_e32 v2, v2
	v_rcp_f32_e32 v3, v3
	v_mul_f32_e32 v0, 0x4038aa3b, v0
	v_mul_f32_e32 v1, 0x4038aa3b, v1
	v_exp_f32_e32 v0, v0
	v_exp_f32_e32 v1, v1
	v_pk_fma_f32 v[22:23], v[2:3], -2.0, 1.0 op_sel_hi:[1,0,0]
	v_cvt_pk_bf16_f32 v2, v28, v29
	v_cvt_pk_bf16_f32 v3, v30, v31
	v_cvt_pk_bf16_f32 v14, v14, v15
	v_cvt_pk_bf16_f32 v15, v16, v17
	v_cvt_pk_bf16_f32 v17, v22, v23
	ds_read_b128 v[22:25], v44 offset:59392
	s_waitcnt lgkmcnt(2)
	v_mfma_f32_16x16x32_bf16 a[0:3], v[10:13], v[2:5], a[8:11]
	ds_read_b128 v[10:13], v44 offset:60416
	v_add_f32_e32 v0, 1.0, v0
	v_add_f32_e32 v1, 1.0, v1
	v_rcp_f32_e32 v0, v0
	v_rcp_f32_e32 v1, v1
	v_cvt_pk_bf16_f32 v7, v38, v39
	v_cvt_pk_bf16_f32 v8, v40, v41
	v_cvt_pk_bf16_f32 v9, v42, v43
	v_pk_fma_f32 v[0:1], v[0:1], -2.0, 1.0 op_sel_hi:[1,0,0]
	s_waitcnt lgkmcnt(0)
	v_mfma_f32_16x16x32_bf16 a[8:11], v[10:13], v[2:5], a[20:23]
	v_cvt_pk_bf16_f32 v16, v0, v1
	v_mov_b32_e32 v0, 0x11000
	v_mad_u32_u24 v0, v56, s0, v0
	v_mfma_f32_16x16x32_bf16 a[0:3], v[18:21], v[6:9], a[0:3]
	ds_read_b128 v[18:21], v44 offset:61440
	v_mad_u32_u24 v1, v57, s2, v0
	v_add_u32_e32 v26, v1, v48
	v_mfma_f32_16x16x32_bf16 a[0:3], v[22:25], v[14:17], a[0:3]
	ds_read_b128 v[22:25], v44 offset:62464
	s_waitcnt lgkmcnt(1)
	v_mfma_f32_16x16x32_bf16 a[8:11], v[18:21], v[6:9], a[8:11]
	ds_read_b128 v[18:21], v44 offset:64512
	s_nop 3
	v_accvgpr_read_b32 v27, a1
	v_accvgpr_read_b32 v10, a0
	ds_write2_b32 v26, v10, v27 offset0:1 offset1:2
	v_accvgpr_read_b32 v10, a3
	v_accvgpr_read_b32 v11, a2
	ds_write2_b32 v26, v11, v10 offset0:3 offset1:4
	ds_read_b128 v[10:13], v44 offset:63488
	s_waitcnt lgkmcnt(4)
	v_mfma_f32_16x16x32_bf16 a[0:3], v[22:25], v[14:17], a[8:11]
	s_nop 7
	v_accvgpr_read_b32 v22, a1
	v_accvgpr_read_b32 v23, a0
	ds_write2_b32 v26, v23, v22 offset0:17 offset1:18
	v_or_b32_e32 v22, 0x10000, v44
	ds_read_b128 v[22:25], v22
	s_waitcnt lgkmcnt(2)
	v_mfma_f32_16x16x32_bf16 a[8:11], v[10:13], v[2:5], a[12:15]
	v_or_b32_e32 v10, 0x10400, v44
	ds_read_b128 v[10:13], v10
	v_accvgpr_read_b32 v27, a3
	v_mfma_f32_16x16x32_bf16 a[8:11], v[18:21], v[6:9], a[8:11]
	v_or_b32_e32 v18, 0x10800, v44
	ds_read_b128 v[18:21], v18
	v_accvgpr_read_b32 v28, a2
	s_waitcnt lgkmcnt(2)
	v_mfma_f32_16x16x32_bf16 a[0:3], v[22:25], v[14:17], a[8:11]
	v_or_b32_e32 v22, 0x10c00, v44
	ds_read_b128 v[22:25], v22
	ds_write2_b32 v26, v28, v27 offset0:19 offset1:20
	s_waitcnt lgkmcnt(3)
	v_mfma_f32_16x16x32_bf16 a[4:7], v[10:13], v[2:5], a[4:7]
	s_waitcnt lgkmcnt(2)
	v_mfma_f32_16x16x32_bf16 a[4:7], v[18:21], v[6:9], a[4:7]
	s_nop 0
	v_accvgpr_read_b32 v2, a1
	v_accvgpr_read_b32 v3, a0
	ds_write2_b32 v26, v3, v2 offset0:33 offset1:34
	v_accvgpr_read_b32 v2, a3
	v_accvgpr_read_b32 v3, a2
	s_waitcnt lgkmcnt(2)
	v_mfma_f32_16x16x32_bf16 a[0:3], v[22:25], v[14:17], a[4:7]
	ds_write2_b32 v26, v3, v2 offset0:35 offset1:36
	s_nop 6
	v_accvgpr_read_b32 v2, a1
	v_accvgpr_read_b32 v3, a0
	ds_write2_b32 v26, v3, v2 offset0:49 offset1:50
	v_accvgpr_read_b32 v2, a3
	v_accvgpr_read_b32 v3, a2
	ds_write2_b32 v26, v3, v2 offset0:51 offset1:52
	s_and_saveexec_b64 s[0:1], vcc
	ds_write_b32 v1, v46
	s_or_b64 exec, exec, s[0:1]
	v_add_u32_e32 v2, v0, v44
	v_mov_b64_e32 v[0:1], s[10:11]
	v_mad_u64_u32 v[0:1], s[0:1], v47, s2, v[0:1]
	ds_read_b128 v[4:7], v2
	v_lshl_add_u64 v[8:9], v[0:1], 0, v[44:45]
	s_waitcnt lgkmcnt(0)
	global_store_dwordx4 v[8:9], v[4:7], off sc1
	s_nop 1
	s_mov_b64 s[0:1], 0x400
	ds_read_b128 v[4:7], v2 offset:1024
	v_lshl_add_u64 v[10:11], v[8:9], 0, s[0:1]
	s_waitcnt lgkmcnt(0)
	global_store_dwordx4 v[10:11], v[4:7], off sc1
	s_nop 1
	s_mov_b64 s[0:1], 0x800
	ds_read_b128 v[4:7], v2 offset:2048
	v_lshl_add_u64 v[10:11], v[8:9], 0, s[0:1]
	s_waitcnt lgkmcnt(0)
	global_store_dwordx4 v[10:11], v[4:7], off sc1
	s_nop 1
	s_mov_b64 s[0:1], 0xc00
	ds_read_b128 v[4:7], v2 offset:3072
	v_lshl_add_u64 v[8:9], v[8:9], 0, s[0:1]
	s_waitcnt lgkmcnt(0)
	global_store_dwordx4 v[8:9], v[4:7], off sc1
	s_nop 1
	v_or_b32_e32 v3, 0x100, v49
	v_cmp_gt_u32_e32 vcc, s2, v3
	s_and_saveexec_b64 s[0:1], vcc
	s_cbranch_execz .LBB2_4
	ds_read_b128 v[4:7], v2 offset:4096
	v_lshlrev_b32_e32 v2, 4, v3
	v_mov_b32_e32 v3, 0
	v_lshl_add_u64 v[0:1], v[0:1], 0, v[2:3]
	s_waitcnt lgkmcnt(0)
	global_store_dwordx4 v[0:1], v[4:7], off sc1
	s_nop 1
